# proj epilogue tail: emax wave reduction via DPP+readlane instead of six ds_bpermute round trips; redundant sum(va) butterfly only in workgroups 0-7
# baseline (speedup 1.0000x reference)
_Z11proj_kernelPKfS0_S0_S0_S0_S0_S0_S0_S0_S0_S0_S0_S0_PfS1_PDF16_S1_S0_S0_S2_:
	s_mov_b32 s88, s2
	s_load_dwordx2 s[16:17], s[0:1], 0x90
	s_load_dwordx4 s[4:7], s[0:1], 0x80
	s_cmpk_gt_u32 s2, 0x5f
	s_mov_b64 s[8:9], -1
	s_cbranch_scc0 .LBB0_16
	s_load_dwordx4 s[8:11], s[0:1], 0x58
	s_lshr_b32 s3, s2, 3
	s_cmpk_gt_u32 s2, 0xbf
	s_mov_b64 s[12:13], -1
	s_cbranch_scc0 .LBB0_3
	v_lshlrev_b32_e32 v54, 2, v0
	v_mov_b32_e32 v55, 0
	s_waitcnt lgkmcnt(0)
	v_lshl_add_u64 v[2:3], s[6:7], 0, v[54:55]
	v_lshl_add_u64 v[4:5], s[16:17], 0, v[54:55]
	v_cmp_gt_u32_e32 vcc, 64, v0
	s_load_dwordx4 s[12:15], s[0:1], 0x38
	s_load_dwordx2 s[22:23], s[0:1], 0x10
	v_cndmask_b32_e32 v2, v4, v2, vcc
	v_cndmask_b32_e32 v3, v5, v3, vcc
	global_load_dword v70, v[2:3], off
	v_lshrrev_b32_e32 v2, 2, v0
	v_and_b32_e32 v56, 15, v0
	v_and_b32_e32 v18, 48, v2
	v_or_b32_e32 v68, v18, v56
	v_bfe_u32 v1, v0, 4, 2
	v_lshlrev_b32_e32 v2, 8, v68
	v_mov_b32_e32 v3, v55
	s_lshl_b32 s20, s2, 1
	v_lshl_add_u64 v[2:3], s[8:9], 0, v[2:3]
	v_lshlrev_b32_e32 v4, 5, v1
	v_mov_b32_e32 v5, v55
	s_and_b32 s20, s20, 6
	s_bfe_u32 s21, s2, 0x10003
	v_lshl_add_u64 v[14:15], v[2:3], 0, v[4:5]
	s_sub_i32 s19, s3, 24
	s_or_b32 s21, s21, s20
	global_load_dwordx4 v[2:5], v[14:15], off
	v_lshl_add_u64 v[6:7], v[14:15], 0, 16
	s_mov_b64 s[24:25], 0x80
	s_bfe_u32 s18, s2, 0x10002
	s_lshr_b32 s19, s19, 1
	s_lshl_b32 s20, s21, 6
	global_load_dwordx4 v[6:9], v[6:7], off
	v_lshl_add_u64 v[10:11], v[14:15], 0, s[24:25]
	s_mov_b64 s[24:25], 0x90
	v_lshlrev_b32_e32 v22, 2, v18
	v_mov_b32_e32 v23, v55
	s_lshl_b32 s21, s21, 8
	global_load_dwordx4 v[10:13], v[10:11], off
	v_lshl_add_u64 v[14:15], v[14:15], 0, s[24:25]
	v_lshl_add_u64 v[24:25], s[10:11], 0, v[22:23]
	v_lshlrev_b32_e32 v18, 4, v1
	v_mov_b32_e32 v19, v55
	s_waitcnt lgkmcnt(0)
	s_add_u32 s14, s14, s21
	global_load_dwordx4 v[14:17], v[14:15], off
	v_lshl_add_u64 v[18:19], v[24:25], 0, v[18:19]
	s_addc_u32 s15, s15, 0
	global_load_dwordx4 v[18:21], v[18:19], off
	v_lshlrev_b32_e32 v26, 2, v56
	v_mov_b32_e32 v27, v55
	v_lshl_add_u64 v[22:23], s[14:15], 0, v[22:23]
	s_mul_i32 s26, s18, 0x180
	v_lshrrev_b32_e32 v57, 4, v0
	v_lshl_add_u64 v[24:25], v[24:25], 0, v[26:27]
	global_load_dword v71, v[24:25], off
	v_lshl_add_u64 v[22:23], v[22:23], 0, v[26:27]
	s_mulk_i32 s19, 0x60
	global_load_dword v69, v[22:23], off
	v_or_b32_e32 v22, s26, v57
	v_add_u32_e32 v22, s19, v22
	v_mov_b32_e32 v23, v55
	v_lshlrev_b64 v[22:23], 11, v[22:23]
	v_and_b32_e32 v72, 60, v54
	v_lshl_add_u64 v[22:23], s[22:23], 0, v[22:23]
	v_lshlrev_b32_e32 v54, 2, v72
	v_lshl_add_u64 v[66:67], v[22:23], 0, v[54:55]
	global_load_dwordx4 v[22:25], v[66:67], off
	s_mov_b32 s14, 0x10000
	v_add_co_u32_e32 v64, vcc, s14, v66
	s_mov_b32 s15, 0x20000
	s_nop 0
	v_addc_co_u32_e32 v65, vcc, 0, v67, vcc
	global_load_dwordx4 v[30:33], v[64:65], off
	v_add_co_u32_e32 v62, vcc, s15, v66
	v_or_b32_e32 v26, s20, v57
	s_nop 0
	v_addc_co_u32_e32 v63, vcc, 0, v67, vcc
	global_load_dwordx4 v[34:37], v[62:63], off
	v_lshlrev_b32_e32 v26, 9, v26
	v_lshl_add_u64 v[26:27], v[26:27], 2, s[12:13]
	v_lshl_add_u64 v[60:61], v[26:27], 0, v[54:55]
	v_add_co_u32_e32 v58, vcc, s14, v60
	global_load_dwordx4 v[38:41], v[60:61], off
	s_nop 0
	v_addc_co_u32_e32 v59, vcc, 0, v61, vcc
	global_load_dwordx4 v[42:45], v[58:59], off
	global_load_dwordx4 v[46:49], v[66:67], off offset:256
	global_load_dwordx4 v[50:53], v[64:65], off offset:256
	global_load_dwordx4 v[74:77], v[62:63], off offset:256
	global_load_dwordx4 v[78:81], v[60:61], off offset:256
	global_load_dwordx4 v[82:85], v[58:59], off offset:256
	global_load_dwordx4 v[86:89], v[66:67], off offset:512
	global_load_dwordx4 v[90:93], v[64:65], off offset:512
	v_lshrrev_b32_e32 v26, 8, v0
	v_mul_u32_u24_e32 v54, 48, v26
	global_load_dwordx4 v[26:29], v[62:63], off offset:512
	global_load_dwordx4 v[94:97], v[60:61], off offset:512
	v_or_b32_e32 v102, v54, v56
	v_and_b32_e32 v56, 48, v0
	s_movk_i32 s14, 0x90
	v_mad_u32_u24 v73, v68, s14, v56
	v_lshl_or_b32 v1, v1, 2, v54
	v_mul_lo_u32 v1, v1, s14
	v_lshl_add_u32 v1, v68, 1, v1
	s_movk_i32 s15, 0x180
	s_waitcnt vmcnt(13)
	v_cvt_f16_f32_e32 v22, v22
	v_cvt_f16_f32_e32 v25, v25
	v_cvt_pk_f16_f32 v23, v23, v24
	v_mul_u32_u24_e32 v24, 0x90, v57
	v_pack_b32_f16 v22, v22, v23
	v_alignbit_b32 v23, v25, v23, 16
	v_lshl_add_u32 v72, v72, 1, v24
	s_waitcnt vmcnt(12)
	v_cvt_f16_f32_e32 v25, v30
	v_cvt_f16_f32_e32 v30, v33
	v_cvt_pk_f16_f32 v31, v31, v32
	v_mad_u64_u32 v[56:57], s[12:13], v102, s14, v[56:57]
	v_pack_b32_f16 v24, v25, v31
	v_alignbit_b32 v25, v30, v31, 16
	s_waitcnt vmcnt(11)
	v_cvt_f16_f32_e32 v30, v34
	ds_write2st64_b64 v72, v[22:23], v[24:25] offset1:9
	s_waitcnt vmcnt(8)
	v_cvt_f16_f32_e32 v34, v46
	v_cvt_pk_f16_f32 v23, v35, v36
	v_cvt_f16_f32_e32 v35, v49
	v_cvt_pk_f16_f32 v36, v47, v48
	v_pack_b32_f16 v102, v34, v36
	s_waitcnt vmcnt(7)
	v_cvt_f16_f32_e32 v34, v50
	v_alignbit_b32 v103, v35, v36, 16
	v_cvt_f16_f32_e32 v35, v53
	v_cvt_pk_f16_f32 v36, v51, v52
	v_pack_b32_f16 v104, v34, v36
	s_waitcnt vmcnt(6)
	v_cvt_f16_f32_e32 v34, v74
	v_alignbit_b32 v105, v35, v36, 16
	v_cvt_f16_f32_e32 v35, v77
	v_cvt_pk_f16_f32 v36, v75, v76
	v_pack_b32_f16 v106, v34, v36
	s_waitcnt vmcnt(5)
	v_cvt_f16_f32_e32 v34, v78
	v_alignbit_b32 v107, v35, v36, 16
	v_cvt_f16_f32_e32 v35, v81
	v_cvt_pk_f16_f32 v36, v79, v80
	v_pack_b32_f16 v108, v34, v36
	s_waitcnt vmcnt(4)
	v_cvt_f16_f32_e32 v34, v82
	v_cvt_f16_f32_e32 v24, v37
	v_pack_b32_f16 v22, v30, v23
	v_cvt_f16_f32_e32 v25, v38
	v_cvt_f16_f32_e32 v30, v41
	v_alignbit_b32 v109, v35, v36, 16
	v_cvt_f16_f32_e32 v35, v85
	v_cvt_pk_f16_f32 v36, v83, v84
	v_cvt_pk_f16_f32 v31, v39, v40
	v_pack_b32_f16 v110, v34, v36
	s_waitcnt vmcnt(3)
	v_cvt_f16_f32_e32 v34, v86
	v_alignbit_b32 v23, v24, v23, 16
	v_pack_b32_f16 v24, v25, v31
	v_alignbit_b32 v25, v30, v31, 16
	v_cvt_f16_f32_e32 v30, v42
	v_cvt_f16_f32_e32 v31, v45
	v_alignbit_b32 v111, v35, v36, 16
	v_cvt_pk_f16_f32 v36, v87, v88
	v_cvt_pk_f16_f32 v32, v43, v44
	v_cvt_f16_f32_e32 v35, v89
	v_pack_b32_f16 v114, v34, v36
	s_waitcnt vmcnt(2)
	v_cvt_f16_f32_e32 v34, v90
	v_pack_b32_f16 v30, v30, v32
	v_alignbit_b32 v31, v31, v32, 16
	ds_write2st64_b64 v72, v[22:23], v[24:25] offset0:18 offset1:54
	global_load_dwordx4 v[22:25], v[58:59], off offset:512
	ds_write_b64 v72, v[30:31] offset:32256
	s_waitcnt lgkmcnt(0)
	s_barrier
	global_load_dwordx4 v[30:33], v[66:67], off offset:768
	global_load_dwordx4 v[98:101], v[64:65], off offset:768
	v_cvt_pk_f16_f32 v39, v91, v92
	v_alignbit_b32 v115, v35, v36, 16
	v_cvt_f16_f32_e32 v38, v93
	v_pack_b32_f16 v116, v34, v39
	ds_read_b128 v[34:37], v56
	s_waitcnt vmcnt(4)
	v_cvt_f16_f32_e32 v57, v26
	v_alignbit_b32 v117, v38, v39, 16
	ds_read_b128 v[38:41], v56 offset:2304
	ds_read_b128 v[46:49], v73 offset:27648
	ds_read_b128 v[50:53], v56 offset:4608
	ds_read_b128 v[74:77], v56 offset:64
	ds_read_b128 v[78:81], v73 offset:27712
	v_cvt_f16_f32_e32 v87, v29
	s_waitcnt lgkmcnt(3)
	v_mfma_f32_16x16x32_f16 v[34:37], v[34:37], v[46:49], 0
	v_cvt_pk_f16_f32 v86, v27, v28
	global_load_dwordx4 v[42:45], v[62:63], off offset:768
	ds_read_b128 v[26:29], v56 offset:2368
	v_mfma_f32_16x16x32_f16 v[82:85], v[38:41], v[46:49], 0
	v_pack_b32_f16 v118, v57, v86
	v_alignbit_b32 v119, v87, v86, 16
	ds_read_b128 v[86:89], v56 offset:4672
	s_waitcnt lgkmcnt(4)
	v_mfma_f32_16x16x32_f16 v[50:53], v[50:53], v[46:49], 0
	global_load_dwordx4 v[46:49], v[60:61], off offset:768
	ds_write2st64_b64 v72, v[102:103], v[104:105] offset0:27 offset1:36
	ds_write2st64_b64 v72, v[106:107], v[108:109] offset0:45 offset1:72
	ds_write_b64 v72, v[110:111] offset:41472
	s_waitcnt lgkmcnt(5)
	v_mfma_f32_16x16x32_f16 v[74:77], v[74:77], v[78:81], v[34:37]
	s_waitcnt vmcnt(5)
	v_cvt_f16_f32_e32 v57, v94
	v_cvt_f16_f32_e32 v90, v97
	v_cvt_pk_f16_f32 v91, v95, v96
	global_load_dwordx4 v[34:37], v[58:59], off offset:768
	s_waitcnt lgkmcnt(0)
	s_barrier
	global_load_dwordx4 v[38:41], v[66:67], off offset:1024
	v_pack_b32_f16 v120, v57, v91
	v_alignbit_b32 v121, v90, v91, 16
	global_load_dwordx4 v[90:93], v[64:65], off offset:1024
	v_mfma_f32_16x16x32_f16 v[50:53], v[86:89], v[78:81], v[50:53]
	global_load_dwordx4 v[86:89], v[62:63], off offset:1024
	s_load_dwordx2 s[12:13], s[0:1], 0x78
	s_waitcnt vmcnt(8)
	v_cvt_f16_f32_e32 v22, v22
	v_mfma_f32_16x16x32_f16 v[82:85], v[26:29], v[78:81], v[82:85]
	v_cvt_f16_f32_e32 v25, v25
	v_cvt_pk_f16_f32 v23, v23, v24
	v_pack_b32_f16 v122, v22, v23
	s_waitcnt vmcnt(7)
	v_cvt_f16_f32_e32 v26, v30
	v_cvt_pk_f16_f32 v57, v31, v32
	v_alignbit_b32 v123, v25, v23, 16
	ds_read_b128 v[22:25], v56 offset:13824
	ds_read_b128 v[78:81], v73 offset:36864
	v_cvt_f16_f32_e32 v125, v33
	s_waitcnt vmcnt(6)
	v_cvt_f16_f32_e32 v126, v98
	v_cvt_pk_f16_f32 v127, v99, v100
	v_cvt_f16_f32_e32 v128, v101
	ds_read_b128 v[94:97], v56 offset:13888
	ds_read_b128 v[98:101], v73 offset:36928
	ds_read_b128 v[30:33], v56 offset:16128
	ds_read_b128 v[102:105], v56 offset:16192
	ds_read_b128 v[106:109], v56 offset:18432
	ds_read_b128 v[110:113], v56 offset:18496
	ds_write2st64_b64 v72, v[114:115], v[116:117] offset1:9
	global_load_dwordx4 v[114:117], v[60:61], off offset:1024
	v_pack_b32_f16 v124, v26, v57
	global_load_dwordx4 v[26:29], v[58:59], off offset:1024
	s_waitcnt lgkmcnt(0)
	v_mfma_f32_16x16x32_f16 v[74:77], v[22:25], v[78:81], v[74:77]
	ds_write2st64_b64 v72, v[118:119], v[120:121] offset0:18 offset1:54
	s_waitcnt vmcnt(7)
	v_cvt_f16_f32_e32 v42, v42
	v_cvt_f16_f32_e32 v45, v45
	v_mfma_f32_16x16x32_f16 v[82:85], v[30:33], v[78:81], v[82:85]
	ds_write_b64 v72, v[122:123] offset:32256
	s_waitcnt lgkmcnt(0)
	s_barrier
	global_load_dwordx4 v[22:25], v[66:67], off offset:1280
	global_load_dwordx4 v[30:33], v[64:65], off offset:1280
	v_cvt_pk_f16_f32 v43, v43, v44
	v_alignbit_b32 v125, v125, v57, 16
	v_mfma_f32_16x16x32_f16 v[50:53], v[106:109], v[78:81], v[50:53]
	v_pack_b32_f16 v108, v42, v43
	v_alignbit_b32 v109, v45, v43, 16
	s_waitcnt vmcnt(7)
	v_cvt_f16_f32_e32 v34, v34
	v_cvt_pk_f16_f32 v35, v35, v36
	v_cvt_f16_f32_e32 v36, v37
	v_mfma_f32_16x16x32_f16 v[42:45], v[94:97], v[98:101], v[74:77]
	v_cvt_f16_f32_e32 v57, v46
	s_waitcnt vmcnt(6)
	v_cvt_f16_f32_e32 v37, v41
	v_pack_b32_f16 v106, v126, v127
	v_cvt_f16_f32_e32 v74, v49
	v_cvt_pk_f16_f32 v75, v47, v48
	v_mfma_f32_16x16x32_f16 v[46:49], v[102:105], v[98:101], v[82:85]
	v_pack_b32_f16 v104, v34, v35
	v_cvt_f16_f32_e32 v34, v38
	v_alignbit_b32 v105, v36, v35, 16
	v_cvt_pk_f16_f32 v35, v39, v40
	v_alignbit_b32 v119, v37, v35, 16
	v_pack_b32_f16 v118, v34, v35
	ds_read_b128 v[34:37], v56
	v_pack_b32_f16 v102, v57, v75
	v_alignbit_b32 v103, v74, v75, 16
	ds_read_b128 v[74:77], v56 offset:2304
	ds_read_b128 v[78:81], v73 offset:27648
	s_waitcnt vmcnt(5)
	v_cvt_f16_f32_e32 v38, v90
	v_cvt_f16_f32_e32 v40, v93
	v_mfma_f32_16x16x32_f16 v[50:53], v[110:113], v[98:101], v[50:53]
	v_cvt_pk_f16_f32 v39, v91, v92
	v_pack_b32_f16 v120, v38, v39
	v_alignbit_b32 v121, v40, v39, 16
	ds_read_b128 v[82:85], v56 offset:4608
	ds_read_b128 v[90:93], v56 offset:64
	ds_read_b128 v[94:97], v73 offset:27712
	s_waitcnt lgkmcnt(3)
	v_mfma_f32_16x16x32_f16 v[34:37], v[34:37], v[78:81], v[42:45]
	global_load_dwordx4 v[38:41], v[62:63], off offset:1280
	v_alignbit_b32 v107, v128, v127, 16
	ds_read_b128 v[98:101], v56 offset:2368
	s_waitcnt vmcnt(5)
	v_cvt_f16_f32_e32 v42, v86
	v_cvt_f16_f32_e32 v44, v89
	v_mfma_f32_16x16x32_f16 v[74:77], v[74:77], v[78:81], v[46:49]
	v_cvt_pk_f16_f32 v43, v87, v88
	v_pack_b32_f16 v122, v42, v43
	v_alignbit_b32 v123, v44, v43, 16
	s_waitcnt lgkmcnt(3)
	v_mfma_f32_16x16x32_f16 v[78:81], v[82:85], v[78:81], v[50:53]
	global_load_dwordx4 v[42:45], v[58:59], off offset:1280
	ds_read_b128 v[86:89], v56 offset:4672
	ds_write2st64_b64 v72, v[124:125], v[106:107] offset0:27 offset1:36
	global_load_dwordx4 v[50:53], v[60:61], off offset:1280
	ds_write2st64_b64 v72, v[108:109], v[102:103] offset0:45 offset1:72
	ds_write_b64 v72, v[104:105] offset:41472
	s_waitcnt lgkmcnt(0)
	s_barrier
	global_load_dwordx4 v[46:49], v[66:67], off offset:1536
	global_load_dwordx4 v[82:85], v[64:65], off offset:1536
	v_mfma_f32_16x16x32_f16 v[78:81], v[86:89], v[94:97], v[78:81]
	ds_read_b128 v[86:89], v73 offset:36864
	s_waitcnt vmcnt(8)
	v_cvt_f16_f32_e32 v57, v114
	v_mfma_f32_16x16x32_f16 v[34:37], v[90:93], v[94:97], v[34:37]
	s_waitcnt vmcnt(7)
	v_cvt_f16_f32_e32 v26, v26
	v_cvt_f16_f32_e32 v29, v29
	v_cvt_pk_f16_f32 v27, v27, v28
	v_cvt_f16_f32_e32 v91, v117
	v_pack_b32_f16 v126, v26, v27
	v_alignbit_b32 v127, v29, v27, 16
	ds_read_b128 v[26:29], v56 offset:13824
	v_cvt_pk_f16_f32 v90, v115, v116
	v_pack_b32_f16 v124, v57, v90
	v_mfma_f32_16x16x32_f16 v[74:77], v[98:101], v[94:97], v[74:77]
	v_alignbit_b32 v125, v91, v90, 16
	s_waitcnt vmcnt(5)
	v_cvt_f16_f32_e32 v130, v30
	v_cvt_pk_f16_f32 v131, v31, v32
	v_cvt_f16_f32_e32 v132, v33
	ds_read_b128 v[90:93], v56 offset:13888
	global_load_dwordx4 v[94:97], v[62:63], off offset:1536
	ds_read_b128 v[98:101], v73 offset:36928
	s_waitcnt lgkmcnt(2)
	v_mfma_f32_16x16x32_f16 v[26:29], v[26:29], v[86:89], v[34:37]
	ds_read_b128 v[30:33], v56 offset:16128
	ds_read_b128 v[102:105], v56 offset:16192
	ds_read_b128 v[106:109], v56 offset:18432
	ds_read_b128 v[110:113], v56 offset:18496
	global_load_dwordx4 v[114:117], v[60:61], off offset:1536
	global_load_dwordx4 v[34:37], v[58:59], off offset:1536
	v_cvt_f16_f32_e32 v57, v22
	v_cvt_pk_f16_f32 v128, v23, v24
	v_cvt_f16_f32_e32 v129, v25
	ds_write2st64_b64 v72, v[118:119], v[120:121] offset1:9
	ds_write2st64_b64 v72, v[122:123], v[124:125] offset0:18 offset1:54
	ds_write_b64 v72, v[126:127] offset:32256
	s_waitcnt lgkmcnt(0)
	s_barrier
	global_load_dwordx4 v[22:25], v[66:67], off offset:1792
	v_mfma_f32_16x16x32_f16 v[74:77], v[30:33], v[86:89], v[74:77]
	global_load_dwordx4 v[30:33], v[64:65], off offset:1792
	v_pack_b32_f16 v118, v57, v128
	v_alignbit_b32 v119, v129, v128, 16
	v_mfma_f32_16x16x32_f16 v[64:67], v[106:109], v[86:89], v[78:81]
	v_pack_b32_f16 v120, v130, v131
	v_alignbit_b32 v121, v132, v131, 16
	s_waitcnt vmcnt(9)
	v_cvt_f16_f32_e32 v38, v38
	v_cvt_f16_f32_e32 v41, v41
	v_cvt_pk_f16_f32 v39, v39, v40
	v_mfma_f32_16x16x32_f16 v[78:81], v[90:93], v[98:101], v[26:29]
	v_pack_b32_f16 v106, v38, v39
	v_alignbit_b32 v107, v41, v39, 16
	s_waitcnt vmcnt(8)
	v_cvt_f16_f32_e32 v38, v42
	v_cvt_f16_f32_e32 v40, v45
	v_cvt_pk_f16_f32 v39, v43, v44
	s_waitcnt vmcnt(7)
	v_cvt_f16_f32_e32 v26, v50
	v_cvt_f16_f32_e32 v27, v53
	v_cvt_pk_f16_f32 v28, v51, v52
	v_mfma_f32_16x16x32_f16 v[50:53], v[102:105], v[98:101], v[74:77]
	v_pack_b32_f16 v102, v26, v28
	v_alignbit_b32 v103, v27, v28, 16
	global_load_dwordx4 v[26:29], v[62:63], off offset:1792
	v_pack_b32_f16 v104, v38, v39
	s_waitcnt vmcnt(7)
	v_cvt_f16_f32_e32 v38, v46
	v_alignbit_b32 v105, v40, v39, 16
	v_cvt_f16_f32_e32 v39, v49
	s_waitcnt vmcnt(6)
	v_cvt_f16_f32_e32 v44, v82
	v_cvt_pk_f16_f32 v40, v47, v48
	v_cvt_pk_f16_f32 v48, v83, v84
	v_pack_b32_f16 v38, v38, v40
	v_alignbit_b32 v39, v39, v40, 16
	ds_read_b128 v[40:43], v56
	v_pack_b32_f16 v108, v44, v48
	v_cvt_f16_f32_e32 v49, v85
	ds_read_b128 v[44:47], v56 offset:2304
	ds_read_b128 v[74:77], v73 offset:27648
	ds_read_b128 v[82:85], v56 offset:4608
	global_load_dwordx4 v[60:63], v[60:61], off offset:1792
	v_mfma_f32_16x16x32_f16 v[64:67], v[110:113], v[98:101], v[64:67]
	ds_read_b128 v[86:89], v56 offset:64
	ds_read_b128 v[90:93], v73 offset:27712
	global_load_dwordx4 v[98:101], v[58:59], off offset:1792
	v_alignbit_b32 v109, v49, v48, 16
	s_waitcnt lgkmcnt(3)
	v_mfma_f32_16x16x32_f16 v[40:43], v[40:43], v[74:77], v[78:81]
	s_waitcnt vmcnt(7)
	v_cvt_pk_f16_f32 v57, v95, v96
	s_nop 0
	ds_read_b128 v[78:81], v56 offset:2368
	v_mfma_f32_16x16x32_f16 v[44:47], v[44:47], v[74:77], v[50:53]
	s_waitcnt vmcnt(6)
	v_cvt_f16_f32_e32 v59, v117
	s_waitcnt vmcnt(5)
	v_cvt_f16_f32_e32 v34, v34
	ds_read_b128 v[48:51], v56 offset:4672
	v_cvt_f16_f32_e32 v52, v94
	v_cvt_f16_f32_e32 v53, v97
	v_cvt_f16_f32_e32 v37, v37
	v_cvt_pk_f16_f32 v35, v35, v36
	s_waitcnt lgkmcnt(4)
	v_mfma_f32_16x16x32_f16 v[64:67], v[82:85], v[74:77], v[64:67]
	v_pack_b32_f16 v52, v52, v57
	v_alignbit_b32 v53, v53, v57, 16
	v_cvt_f16_f32_e32 v57, v114
	s_waitcnt lgkmcnt(2)
	v_mfma_f32_16x16x32_f16 v[40:43], v[86:89], v[90:93], v[40:43]
	ds_write2st64_b64 v72, v[118:119], v[120:121] offset0:27 offset1:36
	ds_write2st64_b64 v72, v[106:107], v[102:103] offset0:45 offset1:72
	ds_write_b64 v72, v[104:105] offset:41472
	v_pack_b32_f16 v86, v34, v35
	v_alignbit_b32 v87, v37, v35, 16
	s_waitcnt lgkmcnt(0)
	s_barrier
	ds_read_b128 v[34:37], v56 offset:13824
	v_cvt_pk_f16_f32 v74, v115, v116
	v_pack_b32_f16 v58, v57, v74
	v_alignbit_b32 v59, v59, v74, 16
	v_mfma_f32_16x16x32_f16 v[48:51], v[48:51], v[90:93], v[64:67]
	s_nop 2
	ds_read_b128 v[64:67], v56 offset:16128
	ds_read_b128 v[74:77], v73 offset:36864
	s_waitcnt vmcnt(4)
	v_cvt_f16_f32_e32 v57, v22
	v_cvt_pk_f16_f32 v89, v23, v24
	v_mfma_f32_16x16x32_f16 v[44:47], v[78:81], v[90:93], v[44:47]
	v_cvt_f16_f32_e32 v90, v25
	ds_read_b128 v[22:25], v56 offset:18432
	ds_read_b128 v[78:81], v56 offset:13888
	ds_read_b128 v[82:85], v73 offset:36928
	s_waitcnt vmcnt(3)
	v_cvt_f16_f32_e32 v30, v30
	s_waitcnt lgkmcnt(3)
	v_mfma_f32_16x16x32_f16 v[34:37], v[34:37], v[74:77], v[40:43]
	v_cvt_f16_f32_e32 v33, v33
	v_cvt_pk_f16_f32 v31, v31, v32
	v_pack_b32_f16 v88, v57, v89
	ds_read_b128 v[40:43], v56 offset:16192
	v_mfma_f32_16x16x32_f16 v[44:47], v[64:67], v[74:77], v[44:47]
	ds_read_b128 v[64:67], v56 offset:18496
	v_alignbit_b32 v89, v90, v89, 16
	v_pack_b32_f16 v90, v30, v31
	s_waitcnt lgkmcnt(4)
	v_mfma_f32_16x16x32_f16 v[22:25], v[22:25], v[74:77], v[48:51]
	v_alignbit_b32 v91, v33, v31, 16
	ds_write2st64_b64 v72, v[38:39], v[108:109] offset1:9
	ds_write2st64_b64 v72, v[52:53], v[58:59] offset0:18 offset1:54
	ds_write_b64 v72, v[86:87] offset:32256
	s_waitcnt lgkmcnt(0)
	v_mfma_f32_16x16x32_f16 v[30:33], v[78:81], v[82:85], v[34:37]
	s_barrier
	s_waitcnt vmcnt(2)
	v_cvt_f16_f32_e32 v57, v26
	ds_read_b128 v[34:37], v56
	v_mfma_f32_16x16x32_f16 v[38:41], v[40:43], v[82:85], v[44:47]
	s_nop 2
	ds_read_b128 v[42:45], v56 offset:2304
	ds_read_b128 v[46:49], v73 offset:27648
	v_cvt_pk_f16_f32 v58, v27, v28
	v_cvt_f16_f32_e32 v59, v29
	v_mfma_f32_16x16x32_f16 v[22:25], v[64:67], v[82:85], v[22:25]
	ds_read_b128 v[50:53], v56 offset:4608
	ds_read_b128 v[64:67], v56 offset:64
	ds_read_b128 v[74:77], v73 offset:27712
	ds_read_b128 v[26:29], v56 offset:2368
	s_waitcnt lgkmcnt(4)
	v_mfma_f32_16x16x32_f16 v[30:33], v[34:37], v[46:49], v[30:33]
	v_mfma_f32_16x16x32_f16 v[34:37], v[42:45], v[46:49], v[38:41]
	s_waitcnt vmcnt(1)
	v_cvt_f16_f32_e32 v44, v60
	v_cvt_f16_f32_e32 v45, v63
	v_pack_b32_f16 v42, v57, v58
	s_waitcnt lgkmcnt(3)
	v_mfma_f32_16x16x32_f16 v[22:25], v[50:53], v[46:49], v[22:25]
	v_cvt_pk_f16_f32 v46, v61, v62
	ds_read_b128 v[38:41], v56 offset:4672
	v_pack_b32_f16 v44, v44, v46
	v_alignbit_b32 v45, v45, v46, 16
	s_waitcnt vmcnt(0)
	v_cvt_f16_f32_e32 v46, v98
	s_waitcnt lgkmcnt(1)
	v_mfma_f32_16x16x32_f16 v[26:29], v[26:29], v[74:77], v[34:37]
	v_alignbit_b32 v43, v59, v58, 16
	ds_write2st64_b64 v72, v[88:89], v[90:91] offset0:27 offset1:36
	ds_write2st64_b64 v72, v[42:43], v[44:45] offset0:45 offset1:72
	v_cvt_f16_f32_e32 v35, v101
	v_cvt_pk_f16_f32 v36, v99, v100
	v_pack_b32_f16 v34, v46, v36
	v_mfma_f32_16x16x32_f16 v[30:33], v[64:67], v[74:77], v[30:33]
	v_alignbit_b32 v35, v35, v36, 16
	ds_write_b64 v72, v[34:35] offset:41472
	s_waitcnt lgkmcnt(0)
	s_barrier
	ds_read_b128 v[34:37], v56 offset:13824
	v_mfma_f32_16x16x32_f16 v[22:25], v[38:41], v[74:77], v[22:25]
	ds_read_b128 v[38:41], v73 offset:36864
	ds_read_b128 v[42:45], v56 offset:13888
	ds_read_b128 v[46:49], v73 offset:36928
	s_waitcnt lgkmcnt(2)
	v_mfma_f32_16x16x32_f16 v[30:33], v[34:37], v[38:41], v[30:33]
	ds_read_b128 v[34:37], v56 offset:16128
	ds_read_b128 v[50:53], v56 offset:16192
	s_waitcnt lgkmcnt(2)
	v_mfma_f32_16x16x32_f16 v[30:33], v[42:45], v[46:49], v[30:33]
	s_waitcnt lgkmcnt(1)
	v_mfma_f32_16x16x32_f16 v[26:29], v[34:37], v[38:41], v[26:29]
	ds_read_b128 v[34:37], v56 offset:18432
	ds_read_b128 v[56:59], v56 offset:18496
	s_waitcnt vmcnt(0)
	s_waitcnt lgkmcnt(0)
	s_nop 2
	v_add_f32_e32 v2, v30, v69
	v_mfma_f32_16x16x32_f16 v[26:29], v[50:53], v[46:49], v[26:29]
	v_cvt_f16_f32_e32 v2, v2
	v_add_f32_e32 v3, v31, v69
	v_cvt_f16_f32_e32 v3, v3
	v_mfma_f32_16x16x32_f16 v[22:25], v[34:37], v[38:41], v[22:25]
	v_add_f32_e32 v4, v32, v69
	v_cvt_f16_f32_e32 v4, v4
	v_add_f32_e32 v5, v33, v69
	v_cvt_f16_f32_e32 v5, v5
	s_barrier
	ds_write_b16 v1, v2
	ds_write_b16 v1, v3 offset:144
	ds_write_b16 v1, v4 offset:288
	ds_write_b16 v1, v5 offset:432
	v_add_f32_e32 v2, v26, v69
	v_mfma_f32_16x16x32_f16 v[22:25], v[56:59], v[46:49], v[22:25]
	v_cvt_f16_f32_e32 v2, v2
	v_add_f32_e32 v3, v27, v69
	v_cvt_f16_f32_e32 v3, v3
	v_add_f32_e32 v4, v28, v69
	v_cvt_f16_f32_e32 v4, v4
	v_add_f32_e32 v5, v29, v69
	v_cvt_f16_f32_e32 v5, v5
	ds_write_b16 v1, v2 offset:2304
	ds_write_b16 v1, v3 offset:2448
	ds_write_b16 v1, v4 offset:2592
	ds_write_b16 v1, v5 offset:2736
	v_add_f32_e32 v2, v22, v69
	v_cvt_f16_f32_e32 v2, v2
	v_add_f32_e32 v3, v23, v69
	v_cvt_f16_f32_e32 v3, v3
	v_add_f32_e32 v4, v24, v69
	v_cvt_f16_f32_e32 v4, v4
	v_add_f32_e32 v5, v25, v69
	v_cvt_f16_f32_e32 v5, v5
	ds_write_b16 v1, v2 offset:4608
	ds_write_b16 v1, v3 offset:4752
	ds_write_b16 v1, v4 offset:4896
	ds_write_b16 v1, v5 offset:5040
	v_and_b32_e32 v2, 7, v0
	v_mul_u32_u24_e32 v10, 12, v2
	v_mul_u32_u24_e32 v2, 0x360, v2
	v_lshrrev_b32_e32 v1, 3, v0
	v_lshlrev_b32_e32 v2, 1, v2
	v_lshl_add_u32 v3, v1, 1, v2
	s_waitcnt lgkmcnt(0)
	s_barrier
	ds_read_u16 v2, v3
	ds_read_u16 v4, v3 offset:144
	ds_read_u16 v5, v3 offset:288
	ds_read_u16 v6, v3 offset:432
	ds_read_u16 v7, v3 offset:576
	ds_read_u16 v8, v3 offset:720
	ds_read_u16 v9, v3 offset:864
	ds_read_u16 v11, v3 offset:1008
	ds_read_u16 v12, v3 offset:1152
	ds_read_u16 v13, v3 offset:1296
	ds_read_u16 v14, v3 offset:1440
	ds_read_u16 v15, v3 offset:1584
	v_lshl_or_b32 v1, s18, 9, v1
	s_waitcnt lgkmcnt(10)
	v_lshl_or_b32 v2, v4, 16, v2
	s_waitcnt lgkmcnt(6)
	v_lshl_or_b32 v4, v8, 16, v7
	v_or_b32_e32 v1, s20, v1
	v_mov_b32_e32 v8, s19
	v_mad_u32_u24 v54, v1, s15, v8
	v_lshl_or_b32 v3, v6, 16, v5
	s_waitcnt lgkmcnt(4)
	v_lshl_or_b32 v5, v11, 16, v9
	v_lshl_add_u64 v[8:9], v[54:55], 1, s[12:13]
	v_lshlrev_b32_e32 v54, 1, v10
	v_lshl_add_u64 v[8:9], v[8:9], 0, v[54:55]
	s_waitcnt lgkmcnt(2)
	v_lshl_or_b32 v6, v13, 16, v12
	s_waitcnt lgkmcnt(0)
	v_lshl_or_b32 v7, v15, 16, v14
	global_store_dwordx4 v[8:9], v[2:5], off
	global_store_dwordx2 v[8:9], v[6:7], off offset:16
	s_mov_b64 s[12:13], 0

.LBB0_6:
	s_or_saveexec_b64 s[8:9], s[8:9]
	v_and_b32_e32 v17, 63, v0
	s_xor_b64 exec, exec, s[8:9]
	s_branch .LBB0_10
	v_mbcnt_lo_u32_b32 v1, -1, 0
	v_mbcnt_hi_u32_b32 v1, -1, v1
	v_and_b32_e32 v10, 64, v1
	v_add_u32_e32 v14, 64, v10
	v_xor_b32_e32 v15, 32, v1
	v_cmp_lt_i32_e32 vcc, v15, v14
	v_and_b32_e32 v55, 0x7fffffff, v54
	v_xor_b32_e32 v16, 16, v1
	v_cndmask_b32_e32 v10, v1, v15, vcc
	v_lshlrev_b32_e32 v11, 2, v10
	ds_bpermute_b32 v10, v11, v54
	ds_bpermute_b32 v11, v11, v55
	v_cmp_lt_i32_e32 vcc, v16, v14
	v_xor_b32_e32 v18, 8, v1
	s_waitcnt lgkmcnt(0)
	v_pk_add_f32 v[10:11], v[54:55], v[10:11]
	v_cndmask_b32_e32 v12, v1, v16, vcc
	v_lshlrev_b32_e32 v13, 2, v12
	ds_bpermute_b32 v12, v13, v10
	ds_bpermute_b32 v13, v13, v11
	v_cmp_lt_i32_e32 vcc, v18, v14
	s_waitcnt lgkmcnt(0)
	v_pk_add_f32 v[10:11], v[10:11], v[12:13]
	v_cndmask_b32_e32 v19, v1, v18, vcc
	v_lshlrev_b32_e32 v19, 2, v19
	ds_bpermute_b32 v12, v19, v10
	ds_bpermute_b32 v13, v19, v11
	v_xor_b32_e32 v19, 4, v1
	v_cmp_lt_i32_e32 vcc, v19, v14
	s_waitcnt lgkmcnt(0)
	v_pk_add_f32 v[10:11], v[10:11], v[12:13]
	v_cndmask_b32_e32 v20, v1, v19, vcc
	v_lshlrev_b32_e32 v20, 2, v20
	ds_bpermute_b32 v12, v20, v10
	ds_bpermute_b32 v13, v20, v11
	v_xor_b32_e32 v20, 2, v1
	v_cmp_lt_i32_e32 vcc, v20, v14
	s_waitcnt lgkmcnt(0)
	v_pk_add_f32 v[10:11], v[10:11], v[12:13]
	v_cndmask_b32_e32 v21, v1, v20, vcc
	v_lshlrev_b32_e32 v21, 2, v21
	ds_bpermute_b32 v12, v21, v10
	ds_bpermute_b32 v13, v21, v11
	v_xor_b32_e32 v21, 1, v1
	v_cmp_lt_i32_e32 vcc, v21, v14
	s_waitcnt lgkmcnt(0)
	v_pk_add_f32 v[10:11], v[10:11], v[12:13]
	v_cndmask_b32_e32 v12, v1, v21, vcc
	v_lshlrev_b32_e32 v13, 2, v12
	ds_bpermute_b32 v12, v13, v10
	ds_bpermute_b32 v13, v13, v11
	v_cmp_eq_u32_e32 vcc, 0, v17
	s_and_saveexec_b64 s[10:11], vcc
	s_cbranch_execz .LBB0_9
	v_mov_b32_e32 v22, 0
	s_waitcnt lgkmcnt(0)
	v_pk_add_f32 v[10:11], v[10:11], v[12:13]
	global_store_dwordx2 v22, v[10:11], s[4:5] offset:1024

.LBB0_10:
	s_or_b64 exec, exec, s[8:9]
	v_max_f32_e32 v9, v9, v9
	v_max_f32_e32 v8, v8, v8
	v_max_f32_e32 v5, v5, v5
	v_max_f32_e32 v4, v4, v4
	v_max_f32_e32 v8, v8, v9
	v_max_f32_e32 v4, v4, v5
	v_max3_f32 v6, v6, v7, v8
	v_max3_f32 v2, v2, v3, v4
	v_max3_f32 v2, v6, 0, v2
	s_nop 1
	v_max_f32_dpp v3, v2, v2 quad_perm:[1,0,3,2] row_mask:0xf bank_mask:0xf
	s_nop 1
	v_max_f32_dpp v2, v3, v3 quad_perm:[2,3,0,1] row_mask:0xf bank_mask:0xf
	s_nop 1
	v_max_f32_dpp v3, v2, v2 row_ror:4 row_mask:0xf bank_mask:0xf
	s_nop 1
	v_max_f32_dpp v2, v3, v3 row_ror:8 row_mask:0xf bank_mask:0xf
	s_nop 1
	v_readlane_b32 s80, v2, 0
	v_readlane_b32 s81, v2, 16
	v_readlane_b32 s82, v2, 32
	v_readlane_b32 s83, v2, 48
	s_nop 1
	v_mov_b32_e32 v2, s80
	s_nop 0
	v_max_f32_e32 v2, s81, v2
	v_max_f32_e32 v2, s82, v2
	v_max_f32_e32 v2, s83, v2
	v_mov_b32_e32 v1, v2
	v_cmp_eq_u32_e32 vcc, 0, v17
	s_and_saveexec_b64 s[8:9], vcc
	s_cbranch_execz .LBB0_12
	v_lshrrev_b32_e32 v3, 6, v0
	s_waitcnt lgkmcnt(0)
	v_max_f32_e32 v1, v1, v1
	v_max_f32_e32 v2, v2, v2
	v_lshlrev_b32_e32 v3, 2, v3
	v_max_f32_e32 v1, v2, v1
	ds_write_b32 v3, v1 offset:46080

.LBB0_16:
	s_andn2_b64 vcc, exec, s[8:9]
	s_cbranch_vccnz .LBB0_27
	v_lshlrev_b32_e32 v24, 2, v0
	v_mov_b32_e32 v25, 0
	v_lshrrev_b32_e32 v1, 2, v0
	s_load_dwordx4 s[12:15], s[0:1], 0x48
	s_load_dwordx4 s[8:11], s[0:1], 0x18
	s_load_dwordx2 s[18:19], s[0:1], 0x0
	v_and_b32_e32 v26, 15, v0
	s_waitcnt lgkmcnt(0)
	v_lshl_add_u64 v[2:3], s[6:7], 0, v[24:25]
	v_lshl_add_u64 v[4:5], s[16:17], 0, v[24:25]
	v_cmp_gt_u32_e32 vcc, 64, v0
	v_and_b32_e32 v18, 48, v1
	v_or_b32_e32 v1, v18, v26
	v_cndmask_b32_e32 v3, v5, v3, vcc
	v_cndmask_b32_e32 v2, v4, v2, vcc
	v_bfe_u32 v23, v0, 4, 2
	global_load_dword v22, v[2:3], off
	v_lshlrev_b32_e32 v2, 8, v1
	v_mov_b32_e32 v3, v25
	v_lshl_add_u64 v[2:3], s[12:13], 0, v[2:3]
	v_lshlrev_b32_e32 v4, 5, v23
	v_mov_b32_e32 v5, v25
	s_lshl_b32 s3, s2, 1
	v_lshl_add_u64 v[10:11], v[2:3], 0, v[4:5]
	s_bfe_u32 s21, s2, 0x10002
	s_lshr_b32 s20, s2, 4
	s_and_b32 s3, s3, 6
	s_bfe_u32 s2, s2, 0x10003
	global_load_dwordx4 v[6:9], v[10:11], off
	v_lshl_add_u64 v[2:3], v[10:11], 0, 16
	s_mov_b64 s[6:7], 0x80
	s_or_b32 s3, s2, s3
	s_lshl_b32 s2, s20, 6
	s_mul_i32 s22, s21, 0x180
	global_load_dwordx4 v[14:17], v[2:3], off
	v_lshl_add_u64 v[2:3], v[10:11], 0, s[6:7]
	s_mov_b64 s[6:7], 0x90
	s_add_i32 s22, s22, s2
	s_lshl_b32 s21, s21, 3
	v_lshl_add_u64 v[10:11], v[10:11], 0, s[6:7]
	v_lshlrev_b32_e32 v28, 2, v18
	v_mov_b32_e32 v29, v25
	s_lshl_b32 s6, s3, 8
	global_load_dwordx4 v[2:5], v[2:3], off
	v_lshl_add_u64 v[30:31], s[14:15], 0, v[28:29]
	v_and_b32_e32 v64, 48, v0
	v_mov_b32_e32 v65, v25
	s_add_u32 s6, s10, s6
	global_load_dwordx4 v[10:13], v[10:11], off
	v_lshl_add_u64 v[18:19], v[30:31], 0, v[64:65]
	s_addc_u32 s7, s11, 0
	global_load_dwordx4 v[18:21], v[18:19], off
	v_lshlrev_b32_e32 v32, 2, v26
	v_mov_b32_e32 v33, v25
	v_lshl_add_u64 v[28:29], s[6:7], 0, v[28:29]
	v_lshrrev_b32_e32 v60, 4, v0
	v_lshl_add_u64 v[30:31], v[30:31], 0, v[32:33]
	global_load_dword v96, v[30:31], off
	v_lshl_add_u64 v[28:29], v[28:29], 0, v[32:33]
	v_or_b32_e32 v27, s22, v60
	global_load_dword v97, v[28:29], off
	v_lshlrev_b32_e32 v28, 11, v27
	v_mov_b32_e32 v29, v25
	v_and_b32_e32 v61, 60, v24
	v_lshl_add_u64 v[28:29], s[18:19], 0, v[28:29]
	v_lshlrev_b32_e32 v24, 2, v61
	v_lshl_add_u64 v[88:89], v[28:29], 0, v[24:25]
	global_load_dwordx4 v[28:31], v[88:89], off
	s_mov_b32 s6, 0x10000
	v_add_co_u32_e32 v90, vcc, s6, v88
	v_lshlrev_b32_e32 v27, 9, v60
	s_nop 0
	v_addc_co_u32_e32 v91, vcc, 0, v89, vcc
	global_load_dwordx4 v[32:35], v[90:91], off
	v_lshl_or_b32 v36, s3, 15, v27
	v_mov_b32_e32 v37, v25
	v_lshl_add_u64 v[36:37], v[36:37], 2, s[8:9]
	v_lshl_add_u64 v[92:93], v[36:37], 0, v[24:25]
	global_load_dwordx4 v[36:39], v[92:93], off
	v_add_co_u32_e32 v94, vcc, s6, v92
	v_lshrrev_b32_e32 v24, 3, v0
	s_nop 0
	v_addc_co_u32_e32 v95, vcc, 0, v93, vcc
	global_load_dwordx4 v[40:43], v[94:95], off
	global_load_dwordx4 v[44:47], v[88:89], off offset:256
	global_load_dwordx4 v[48:51], v[90:91], off offset:256
	global_load_dwordx4 v[52:55], v[92:93], off offset:256
	global_load_dwordx4 v[56:59], v[94:95], off offset:256
	v_and_b32_e32 v24, 32, v24
	v_or_b32_e32 v62, v24, v26
	s_movk_i32 s6, 0x90
	v_mad_u32_u24 v99, v62, s6, v64
	v_mad_u32_u24 v100, v1, s6, v64
	v_lshlrev_b32_e32 v23, 2, v23
	s_load_dwordx2 s[0:1], s[0:1], 0x68
	s_or_b32 s6, s3, s21
	v_cmp_lt_u32_e32 vcc, 63, v0
	s_waitcnt vmcnt(7)
	v_cvt_f16_f32_e32 v27, v28
	v_cvt_f16_f32_e32 v28, v31
	v_cvt_pk_f16_f32 v29, v29, v30
	v_pack_b32_f16 v26, v27, v29
	v_alignbit_b32 v27, v28, v29, 16
	v_mul_u32_u24_e32 v28, 0x90, v60
	s_waitcnt vmcnt(6)
	v_cvt_f16_f32_e32 v29, v32
	v_cvt_f16_f32_e32 v30, v35
	v_cvt_pk_f16_f32 v31, v33, v34
	v_lshl_add_u32 v98, v61, 1, v28
	v_pack_b32_f16 v28, v29, v31
	v_alignbit_b32 v29, v30, v31, 16
	s_waitcnt vmcnt(5)
	v_cvt_f16_f32_e32 v30, v36
	ds_write2st64_b64 v98, v[26:27], v[28:29] offset1:9
	v_cvt_pk_f16_f32 v27, v37, v38
	v_cvt_f16_f32_e32 v28, v39
	v_pack_b32_f16 v26, v30, v27
	s_waitcnt vmcnt(4)
	v_cvt_f16_f32_e32 v29, v40
	v_cvt_f16_f32_e32 v30, v43
	v_cvt_pk_f16_f32 v31, v41, v42
	v_alignbit_b32 v27, v28, v27, 16
	v_pack_b32_f16 v28, v29, v31
	v_alignbit_b32 v29, v30, v31, 16
	ds_write2st64_b64 v98, v[26:27], v[28:29] offset0:54 offset1:63
	global_load_dwordx4 v[26:29], v[88:89], off offset:512
	global_load_dwordx4 v[30:33], v[90:91], off offset:512
	global_load_dwordx4 v[34:37], v[92:93], off offset:512
	global_load_dwordx4 v[38:41], v[94:95], off offset:512
	s_waitcnt vmcnt(7)
	v_cvt_f16_f32_e32 v42, v44
	v_cvt_pk_f16_f32 v43, v45, v46
	v_cvt_f16_f32_e32 v44, v47
	s_waitcnt vmcnt(6)
	v_cvt_f16_f32_e32 v45, v48
	v_cvt_f16_f32_e32 v47, v51
	v_cvt_pk_f16_f32 v46, v49, v50
	s_waitcnt vmcnt(5)
	v_cvt_f16_f32_e32 v48, v52
	v_cvt_pk_f16_f32 v49, v53, v54
	v_cvt_f16_f32_e32 v50, v55
	s_waitcnt vmcnt(4)
	v_cvt_f16_f32_e32 v51, v56
	v_cvt_f16_f32_e32 v53, v59
	v_cvt_pk_f16_f32 v52, v57, v58
	v_pack_b32_f16 v42, v42, v43
	v_alignbit_b32 v43, v44, v43, 16
	v_pack_b32_f16 v44, v45, v46
	v_alignbit_b32 v45, v47, v46, 16
	s_waitcnt lgkmcnt(0)
	s_barrier
	ds_read_b128 v[60:63], v99
	ds_read_b128 v[64:67], v100 offset:27648
	ds_read_b128 v[68:71], v99 offset:64
	ds_read_b128 v[72:75], v100 offset:27712
	ds_read_b128 v[76:79], v99 offset:2304
	ds_read_b128 v[80:83], v99 offset:2368
	v_pack_b32_f16 v46, v48, v49
	v_alignbit_b32 v47, v50, v49, 16
	v_pack_b32_f16 v48, v51, v52
	v_alignbit_b32 v49, v53, v52, 16
	ds_write2st64_b64 v98, v[42:43], v[44:45] offset0:18 offset1:27
	ds_write2st64_b64 v98, v[46:47], v[48:49] offset0:72 offset1:81
	global_load_dwordx4 v[42:45], v[88:89], off offset:768
	global_load_dwordx4 v[46:49], v[90:91], off offset:768
	global_load_dwordx4 v[50:53], v[92:93], off offset:768
	global_load_dwordx4 v[54:57], v[94:95], off offset:768
	s_waitcnt lgkmcnt(6)
	v_mfma_f32_16x16x32_f16 v[60:63], v[60:63], v[64:67], 0
	s_waitcnt lgkmcnt(0)
	s_barrier
	v_mfma_f32_16x16x32_f16 v[60:63], v[68:71], v[72:75], v[60:63]
	ds_read_b128 v[68:71], v99 offset:9216
	s_waitcnt vmcnt(7)
	v_cvt_f16_f32_e32 v26, v26
	v_mfma_f32_16x16x32_f16 v[64:67], v[76:79], v[64:67], 0
	v_cvt_pk_f16_f32 v27, v27, v28
	v_cvt_f16_f32_e32 v28, v29
	s_waitcnt vmcnt(6)
	v_cvt_f16_f32_e32 v29, v30
	v_cvt_pk_f16_f32 v30, v31, v32
	v_cvt_f16_f32_e32 v31, v33
	s_waitcnt vmcnt(5)
	v_cvt_f16_f32_e32 v32, v34
	v_cvt_pk_f16_f32 v33, v35, v36
	v_cvt_f16_f32_e32 v34, v37
	s_waitcnt vmcnt(4)
	v_cvt_f16_f32_e32 v35, v38
	v_cvt_f16_f32_e32 v37, v41
	v_mfma_f32_16x16x32_f16 v[64:67], v[80:83], v[72:75], v[64:67]
	ds_read_b128 v[72:75], v100 offset:36864
	ds_read_b128 v[76:79], v99 offset:9280
	ds_read_b128 v[80:83], v100 offset:36928
	v_cvt_pk_f16_f32 v36, v39, v40
	v_pack_b32_f16 v26, v26, v27
	v_alignbit_b32 v27, v28, v27, 16
	v_pack_b32_f16 v28, v29, v30
	v_alignbit_b32 v29, v31, v30, 16
	s_waitcnt lgkmcnt(2)
	v_mfma_f32_16x16x32_f16 v[58:61], v[68:71], v[72:75], v[60:63]
	ds_read_b128 v[68:71], v99 offset:11520
	ds_read_b128 v[84:87], v99 offset:11584
	v_pack_b32_f16 v30, v32, v33
	v_alignbit_b32 v31, v34, v33, 16
	v_pack_b32_f16 v32, v35, v36
	v_alignbit_b32 v33, v37, v36, 16
	ds_write2st64_b64 v98, v[26:27], v[28:29] offset1:9
	ds_write2st64_b64 v98, v[30:31], v[32:33] offset0:54 offset1:63
	global_load_dwordx4 v[26:29], v[88:89], off offset:1024
	global_load_dwordx4 v[30:33], v[90:91], off offset:1024
	global_load_dwordx4 v[34:37], v[92:93], off offset:1024
	global_load_dwordx4 v[38:41], v[94:95], off offset:1024
	s_waitcnt lgkmcnt(3)
	v_mfma_f32_16x16x32_f16 v[62:65], v[68:71], v[72:75], v[64:67]
	s_waitcnt lgkmcnt(0)
	s_barrier
	s_nop 0
	ds_read_b128 v[66:69], v99
	s_waitcnt vmcnt(7)
	v_cvt_f16_f32_e32 v42, v42
	v_cvt_pk_f16_f32 v43, v43, v44
	v_cvt_f16_f32_e32 v44, v45
	s_waitcnt vmcnt(6)
	v_cvt_f16_f32_e32 v45, v46
	v_cvt_pk_f16_f32 v46, v47, v48
	v_cvt_f16_f32_e32 v47, v49
	v_mfma_f32_16x16x32_f16 v[58:61], v[76:79], v[80:83], v[58:61]
	s_waitcnt vmcnt(5)
	v_cvt_f16_f32_e32 v48, v50
	v_cvt_pk_f16_f32 v49, v51, v52
	v_cvt_f16_f32_e32 v50, v53
	s_waitcnt vmcnt(4)
	v_cvt_f16_f32_e32 v51, v54
	v_cvt_f16_f32_e32 v53, v57
	v_mfma_f32_16x16x32_f16 v[62:65], v[84:87], v[80:83], v[62:65]
	ds_read_b128 v[70:73], v100 offset:27648
	ds_read_b128 v[74:77], v99 offset:64
	ds_read_b128 v[78:81], v100 offset:27712
	v_cvt_pk_f16_f32 v52, v55, v56
	v_pack_b32_f16 v42, v42, v43
	v_alignbit_b32 v43, v44, v43, 16
	v_pack_b32_f16 v44, v45, v46
	v_alignbit_b32 v45, v47, v46, 16
	s_waitcnt lgkmcnt(2)
	v_mfma_f32_16x16x32_f16 v[58:61], v[66:69], v[70:73], v[58:61]
	ds_read_b128 v[66:69], v99 offset:2304
	ds_read_b128 v[82:85], v99 offset:2368
	v_pack_b32_f16 v46, v48, v49
	v_alignbit_b32 v47, v50, v49, 16
	v_pack_b32_f16 v48, v51, v52
	v_alignbit_b32 v49, v53, v52, 16
	ds_write2st64_b64 v98, v[42:43], v[44:45] offset0:18 offset1:27
	ds_write2st64_b64 v98, v[46:47], v[48:49] offset0:72 offset1:81
	global_load_dwordx4 v[42:45], v[88:89], off offset:1280
	global_load_dwordx4 v[46:49], v[90:91], off offset:1280
	global_load_dwordx4 v[50:53], v[92:93], off offset:1280
	global_load_dwordx4 v[54:57], v[94:95], off offset:1280
	s_waitcnt lgkmcnt(3)
	v_mfma_f32_16x16x32_f16 v[62:65], v[66:69], v[70:73], v[62:65]
	s_waitcnt lgkmcnt(0)
	s_barrier
	ds_read_b128 v[66:69], v99 offset:9216
	v_mfma_f32_16x16x32_f16 v[58:61], v[74:77], v[78:81], v[58:61]
	s_waitcnt vmcnt(7)
	v_cvt_f16_f32_e32 v26, v26
	v_mfma_f32_16x16x32_f16 v[62:65], v[82:85], v[78:81], v[62:65]
	ds_read_b128 v[70:73], v100 offset:36864
	ds_read_b128 v[74:77], v99 offset:9280
	ds_read_b128 v[78:81], v100 offset:36928
	v_cvt_pk_f16_f32 v27, v27, v28
	v_cvt_f16_f32_e32 v28, v29
	s_waitcnt vmcnt(6)
	v_cvt_f16_f32_e32 v29, v30
	v_cvt_pk_f16_f32 v30, v31, v32
	v_cvt_f16_f32_e32 v31, v33
	s_waitcnt vmcnt(5)
	v_cvt_f16_f32_e32 v32, v34
	v_cvt_pk_f16_f32 v33, v35, v36
	v_cvt_f16_f32_e32 v34, v37
	s_waitcnt vmcnt(4)
	v_cvt_f16_f32_e32 v35, v38
	v_cvt_f16_f32_e32 v37, v41
	s_waitcnt lgkmcnt(2)
	v_mfma_f32_16x16x32_f16 v[58:61], v[66:69], v[70:73], v[58:61]
	ds_read_b128 v[66:69], v99 offset:11520
	ds_read_b128 v[82:85], v99 offset:11584
	v_cvt_pk_f16_f32 v36, v39, v40
	v_pack_b32_f16 v26, v26, v27
	v_alignbit_b32 v27, v28, v27, 16
	v_pack_b32_f16 v28, v29, v30
	v_alignbit_b32 v29, v31, v30, 16
	v_pack_b32_f16 v30, v32, v33
	v_alignbit_b32 v31, v34, v33, 16
	v_pack_b32_f16 v32, v35, v36
	v_alignbit_b32 v33, v37, v36, 16
	ds_write2st64_b64 v98, v[26:27], v[28:29] offset1:9
	ds_write2st64_b64 v98, v[30:31], v[32:33] offset0:54 offset1:63
	s_waitcnt lgkmcnt(3)
	v_mfma_f32_16x16x32_f16 v[62:65], v[66:69], v[70:73], v[62:65]
	global_load_dwordx4 v[26:29], v[88:89], off offset:1536
	global_load_dwordx4 v[30:33], v[90:91], off offset:1536
	global_load_dwordx4 v[34:37], v[92:93], off offset:1536
	global_load_dwordx4 v[38:41], v[94:95], off offset:1536
	s_waitcnt lgkmcnt(0)
	s_barrier
	ds_read_b128 v[66:69], v99
	v_mfma_f32_16x16x32_f16 v[58:61], v[74:77], v[78:81], v[58:61]
	s_waitcnt vmcnt(6)
	v_cvt_f16_f32_e32 v49, v49
	s_waitcnt vmcnt(5)
	v_cvt_f16_f32_e32 v50, v50
	v_mfma_f32_16x16x32_f16 v[62:65], v[82:85], v[78:81], v[62:65]
	ds_read_b128 v[70:73], v100 offset:27648
	ds_read_b128 v[74:77], v99 offset:64
	ds_read_b128 v[78:81], v100 offset:27712
	global_load_dwordx4 v[82:85], v[88:89], off offset:1792
	ds_read_b128 v[86:89], v99 offset:2368
	s_waitcnt lgkmcnt(3)
	v_mfma_f32_16x16x32_f16 v[58:61], v[66:69], v[70:73], v[58:61]
	ds_read_b128 v[66:69], v99 offset:2304
	v_cvt_pk_f16_f32 v51, v51, v52
	v_cvt_f16_f32_e32 v52, v53
	s_waitcnt lgkmcnt(0)
	v_mfma_f32_16x16x32_f16 v[62:65], v[66:69], v[70:73], v[62:65]
	global_load_dwordx4 v[66:69], v[90:91], off offset:1792
	v_cvt_f16_f32_e32 v70, v42
	v_cvt_f16_f32_e32 v72, v45
	v_cvt_f16_f32_e32 v73, v46
	v_mfma_f32_16x16x32_f16 v[58:61], v[74:77], v[78:81], v[58:61]
	v_cvt_pk_f16_f32 v71, v43, v44
	v_cvt_pk_f16_f32 v74, v47, v48
	global_load_dwordx4 v[42:45], v[92:93], off offset:1792
	v_pack_b32_f16 v46, v70, v71
	v_alignbit_b32 v47, v72, v71, 16
	v_pack_b32_f16 v48, v73, v74
	v_alignbit_b32 v49, v49, v74, 16
	ds_write2st64_b64 v98, v[46:47], v[48:49] offset0:18 offset1:27
	global_load_dwordx4 v[46:49], v[94:95], off offset:1792
	s_waitcnt vmcnt(8)
	v_cvt_f16_f32_e32 v53, v54
	v_cvt_pk_f16_f32 v54, v55, v56
	v_cvt_f16_f32_e32 v55, v57
	v_pack_b32_f16 v50, v50, v51
	v_alignbit_b32 v51, v52, v51, 16
	v_pack_b32_f16 v52, v53, v54
	v_alignbit_b32 v53, v55, v54, 16
	ds_write2st64_b64 v98, v[50:51], v[52:53] offset0:72 offset1:81
	s_waitcnt lgkmcnt(0)
	s_barrier
	ds_read_b128 v[50:53], v99 offset:9216
	v_mfma_f32_16x16x32_f16 v[54:57], v[86:89], v[78:81], v[62:65]
	s_nop 2
	ds_read_b128 v[62:65], v100 offset:36864
	ds_read_b128 v[70:73], v99 offset:9280
	ds_read_b128 v[74:77], v100 offset:36928
	s_waitcnt vmcnt(7)
	v_cvt_f16_f32_e32 v26, v26
	v_cvt_pk_f16_f32 v27, v27, v28
	v_cvt_f16_f32_e32 v28, v29
	s_waitcnt vmcnt(6)
	v_cvt_f16_f32_e32 v29, v30
	v_cvt_pk_f16_f32 v30, v31, v32
	v_cvt_f16_f32_e32 v31, v33
	s_waitcnt vmcnt(5)
	v_cvt_f16_f32_e32 v32, v34
	v_cvt_pk_f16_f32 v33, v35, v36
	v_cvt_f16_f32_e32 v34, v37
	s_waitcnt vmcnt(4)
	v_cvt_f16_f32_e32 v35, v38
	v_cvt_f16_f32_e32 v37, v41
	s_waitcnt lgkmcnt(2)
	v_mfma_f32_16x16x32_f16 v[50:53], v[50:53], v[62:65], v[58:61]
	s_nop 2
	ds_read_b128 v[58:61], v99 offset:11520
	ds_read_b128 v[78:81], v99 offset:11584
	v_cvt_pk_f16_f32 v36, v39, v40
	v_pack_b32_f16 v26, v26, v27
	v_alignbit_b32 v27, v28, v27, 16
	v_pack_b32_f16 v28, v29, v30
	v_alignbit_b32 v29, v31, v30, 16
	s_waitcnt vmcnt(3)
	v_cvt_f16_f32_e32 v38, v82
	v_cvt_f16_f32_e32 v40, v85
	v_pack_b32_f16 v30, v32, v33
	v_alignbit_b32 v31, v34, v33, 16
	v_pack_b32_f16 v32, v35, v36
	v_alignbit_b32 v33, v37, v36, 16
	ds_write2st64_b64 v98, v[26:27], v[28:29] offset1:9
	ds_write2st64_b64 v98, v[30:31], v[32:33] offset0:54 offset1:63
	s_waitcnt lgkmcnt(0)
	s_barrier
	s_waitcnt vmcnt(2)
	v_cvt_f16_f32_e32 v41, v66
	ds_read_b128 v[26:29], v99
	v_mfma_f32_16x16x32_f16 v[54:57], v[58:61], v[62:65], v[54:57]
	v_cvt_pk_f16_f32 v39, v83, v84
	v_cvt_pk_f16_f32 v58, v67, v68
	v_pack_b32_f16 v62, v38, v39
	v_alignbit_b32 v63, v40, v39, 16
	v_pack_b32_f16 v64, v41, v58
	ds_read_b128 v[34:37], v99 offset:2304
	ds_read_b128 v[38:41], v100 offset:27648
	v_mfma_f32_16x16x32_f16 v[30:33], v[70:73], v[74:77], v[50:53]
	v_cvt_f16_f32_e32 v59, v69
	s_waitcnt vmcnt(1)
	v_cvt_f16_f32_e32 v42, v42
	v_cvt_pk_f16_f32 v43, v43, v44
	v_mfma_f32_16x16x32_f16 v[50:53], v[78:81], v[74:77], v[54:57]
	v_cvt_f16_f32_e32 v44, v45
	v_alignbit_b32 v65, v59, v58, 16
	s_nop 0
	ds_read_b128 v[54:57], v99 offset:64
	ds_read_b128 v[58:61], v100 offset:27712
	s_waitcnt lgkmcnt(2)
	v_mfma_f32_16x16x32_f16 v[26:29], v[26:29], v[38:41], v[30:33]
	v_mfma_f32_16x16x32_f16 v[34:37], v[34:37], v[38:41], v[50:53]
	s_waitcnt vmcnt(0)
	v_cvt_f16_f32_e32 v40, v46
	v_cvt_f16_f32_e32 v41, v49
	ds_read_b128 v[30:33], v99 offset:2368
	v_pack_b32_f16 v38, v42, v43
	v_cvt_pk_f16_f32 v42, v47, v48
	v_alignbit_b32 v39, v44, v43, 16
	v_pack_b32_f16 v40, v40, v42
	v_alignbit_b32 v41, v41, v42, 16
	ds_write2st64_b64 v98, v[62:63], v[64:65] offset0:18 offset1:27
	ds_write2st64_b64 v98, v[38:39], v[40:41] offset0:72 offset1:81
	s_waitcnt lgkmcnt(0)
	s_barrier
	ds_read_b128 v[38:41], v99 offset:9216
	v_mfma_f32_16x16x32_f16 v[26:29], v[54:57], v[58:61], v[26:29]
	v_mfma_f32_16x16x32_f16 v[30:33], v[30:33], v[58:61], v[34:37]
	s_nop 2
	ds_read_b128 v[34:37], v100 offset:36864
	ds_read_b128 v[42:45], v99 offset:9280
	ds_read_b128 v[46:49], v100 offset:36928
	s_waitcnt lgkmcnt(2)
	v_mfma_f32_16x16x32_f16 v[26:29], v[38:41], v[34:37], v[26:29]
	ds_read_b128 v[38:41], v99 offset:11520
	ds_read_b128 v[50:53], v99 offset:11584
	s_waitcnt vmcnt(0)
	s_waitcnt lgkmcnt(0)
	v_mfma_f32_16x16x32_f16 v[26:29], v[42:45], v[46:49], v[26:29]
	v_or_b32_e32 v18, v23, v24
	v_mul_u32_u24_e32 v18, 0x90, v18
	v_lshl_add_u32 v18, v1, 1, v18
	v_mfma_f32_16x16x32_f16 v[30:33], v[38:41], v[34:37], v[30:33]
	s_barrier
	s_nop 2
	v_add_f32_e32 v19, v26, v97
	v_cvt_f16_f32_e32 v19, v19
	v_mfma_f32_16x16x32_f16 v[30:33], v[50:53], v[46:49], v[30:33]
	v_add_f32_e32 v20, v27, v97
	v_cvt_f16_f32_e32 v20, v20
	v_add_f32_e32 v21, v28, v97
	v_cvt_f16_f32_e32 v21, v21
	v_add_f32_e32 v26, v29, v97
	v_cvt_f16_f32_e32 v26, v26
	ds_write_b16 v18, v19
	ds_write_b16 v18, v20 offset:144
	ds_write_b16 v18, v21 offset:288
	ds_write_b16 v18, v26 offset:432
	v_add_f32_e32 v19, v30, v97
	v_cvt_f16_f32_e32 v19, v19
	v_add_f32_e32 v20, v31, v97
	v_cvt_f16_f32_e32 v20, v20
	v_add_f32_e32 v21, v32, v97
	v_cvt_f16_f32_e32 v21, v21
	v_add_f32_e32 v26, v33, v97
	v_cvt_f16_f32_e32 v26, v26
	ds_write_b16 v18, v19 offset:2304
	ds_write_b16 v18, v20 offset:2448
	ds_write_b16 v18, v21 offset:2592
	ds_write_b16 v18, v26 offset:2736
	s_waitcnt lgkmcnt(0)
	s_barrier
	ds_read_b128 v[18:21], v99
	v_cvt_pk_f16_f32 v17, v16, v17
	v_cvt_pk_f16_f32 v16, v14, v15
	v_cvt_pk_f16_f32 v15, v8, v9
	v_cvt_pk_f16_f32 v14, v6, v7
	ds_read_b128 v[6:9], v99 offset:64
	ds_read_b128 v[26:29], v99 offset:2304
	ds_read_b128 v[30:33], v99 offset:2368
	s_waitcnt lgkmcnt(3)
	v_mfma_f32_16x16x32_f16 v[18:21], v[18:21], v[14:17], 0
	v_cvt_pk_f16_f32 v13, v12, v13
	v_cvt_pk_f16_f32 v12, v10, v11
	v_cvt_pk_f16_f32 v11, v4, v5
	s_waitcnt lgkmcnt(1)
	v_mfma_f32_16x16x32_f16 v[14:17], v[26:29], v[14:17], 0
	v_cvt_pk_f16_f32 v10, v2, v3
	s_nop 1
	v_mfma_f32_16x16x32_f16 v[2:5], v[6:9], v[10:13], v[18:21]
	s_waitcnt lgkmcnt(0)
	v_mfma_f32_16x16x32_f16 v[6:9], v[30:33], v[10:13], v[14:17]
	v_or3_b32 v12, s2, v24, v23
	v_lshlrev_b32_e32 v24, 3, v1
	v_lshl_add_u64 v[10:11], s[0:1], 0, v[24:25]
	s_nop 2
	v_add_f32_e32 v1, v96, v2
	s_mov_b32 s0, 0xc2200000
	v_mov_b32_e32 v14, 0x42200000
	v_med3_f32 v1, v1, s0, v14
	v_mul_f32_e32 v1, 0x4038aa3b, v1
	v_exp_f32_e32 v2, v1
	v_add_f32_e32 v1, v96, v3
	v_med3_f32 v1, v1, s0, v14
	v_mul_f32_e32 v1, 0x4038aa3b, v1
	s_mul_i32 s2, s6, 0xc0
	v_exp_f32_e32 v3, v1
	v_lshrrev_b32_e32 v1, 1, v12
	v_add_u32_e32 v24, s2, v1
	v_add_f32_e32 v1, v96, v4
	v_med3_f32 v1, v1, s0, v14
	v_mul_f32_e32 v1, 0x4038aa3b, v1
	v_exp_f32_e32 v4, v1
	v_add_f32_e32 v1, v96, v5
	v_med3_f32 v1, v1, s0, v14
	v_mul_f32_e32 v1, 0x4038aa3b, v1
	v_exp_f32_e32 v5, v1
	v_add_f32_e32 v1, v96, v6
	v_med3_f32 v1, v1, s0, v14
	v_mul_f32_e32 v1, 0x4038aa3b, v1
	v_exp_f32_e32 v6, v1
	v_add_f32_e32 v1, v96, v7
	v_med3_f32 v1, v1, s0, v14
	v_mul_f32_e32 v1, 0x4038aa3b, v1
	v_lshlrev_b64 v[12:13], 9, v[24:25]
	v_exp_f32_e32 v7, v1
	v_add_f32_e32 v1, v96, v8
	v_lshl_add_u64 v[12:13], v[10:11], 0, v[12:13]
	v_med3_f32 v1, v1, s0, v14
	global_store_dwordx2 v[12:13], v[2:3], off
	v_or_b32_e32 v12, 1, v24
	v_mov_b32_e32 v13, v25
	v_mul_f32_e32 v1, 0x4038aa3b, v1
	v_lshlrev_b64 v[12:13], 9, v[12:13]
	v_exp_f32_e32 v8, v1
	v_add_f32_e32 v1, v96, v9
	v_lshl_add_u64 v[12:13], v[10:11], 0, v[12:13]
	v_med3_f32 v1, v1, s0, v14
	global_store_dwordx2 v[12:13], v[4:5], off
	v_or_b32_e32 v12, 8, v24
	v_mov_b32_e32 v13, v25
	v_mul_f32_e32 v1, 0x4038aa3b, v1
	v_lshlrev_b64 v[12:13], 9, v[12:13]
	v_exp_f32_e32 v9, v1
	v_lshl_add_u64 v[12:13], v[10:11], 0, v[12:13]
	v_or_b32_e32 v24, 9, v24
	global_store_dwordx2 v[12:13], v[6:7], off
	v_lshlrev_b64 v[12:13], 9, v[24:25]
	v_lshl_add_u64 v[10:11], v[10:11], 0, v[12:13]
	global_store_dwordx2 v[10:11], v[8:9], off
	v_mbcnt_lo_u32_b32 v10, -1, 0
	s_and_saveexec_b64 s[0:1], vcc
	s_xor_b64 s[0:1], exec, s[0:1]
	v_mbcnt_hi_u32_b32 v1, -1, v10
	v_and_b32_e32 v10, 64, v1
	v_add_u32_e32 v14, 64, v10
	v_xor_b32_e32 v15, 32, v1
	v_xor_b32_e32 v16, 16, v1
	v_xor_b32_e32 v18, 8, v1
	v_xor_b32_e32 v19, 4, v1
	v_xor_b32_e32 v20, 2, v1
	v_xor_b32_e32 v21, 1, v1
	s_or_saveexec_b64 s[0:1], s[0:1]
	v_and_b32_e32 v17, 63, v0
	s_xor_b64 exec, exec, s[0:1]
	s_cmp_gt_u32 s88, 7
	s_cbranch_scc1 .LBB0_23
	s_cbranch_execz .LBB0_23
	v_mbcnt_hi_u32_b32 v1, -1, v10
	v_and_b32_e32 v10, 64, v1
	v_add_u32_e32 v14, 64, v10
	v_xor_b32_e32 v15, 32, v1
	v_cmp_lt_i32_e32 vcc, v15, v14
	v_and_b32_e32 v23, 0x7fffffff, v22
	v_xor_b32_e32 v16, 16, v1
	v_cndmask_b32_e32 v10, v1, v15, vcc
	v_lshlrev_b32_e32 v11, 2, v10
	ds_bpermute_b32 v10, v11, v22
	ds_bpermute_b32 v11, v11, v23
	v_cmp_lt_i32_e32 vcc, v16, v14
	v_xor_b32_e32 v18, 8, v1
	s_waitcnt lgkmcnt(0)
	v_pk_add_f32 v[10:11], v[22:23], v[10:11]
	v_cndmask_b32_e32 v12, v1, v16, vcc
	v_lshlrev_b32_e32 v13, 2, v12
	ds_bpermute_b32 v12, v13, v10
	ds_bpermute_b32 v13, v13, v11
	v_cmp_lt_i32_e32 vcc, v18, v14
	s_waitcnt lgkmcnt(0)
	v_pk_add_f32 v[10:11], v[10:11], v[12:13]
	v_cndmask_b32_e32 v19, v1, v18, vcc
	v_lshlrev_b32_e32 v19, 2, v19
	ds_bpermute_b32 v12, v19, v10
	ds_bpermute_b32 v13, v19, v11
	v_xor_b32_e32 v19, 4, v1
	v_cmp_lt_i32_e32 vcc, v19, v14
	s_waitcnt lgkmcnt(0)
	v_pk_add_f32 v[10:11], v[10:11], v[12:13]
	v_cndmask_b32_e32 v20, v1, v19, vcc
	v_lshlrev_b32_e32 v20, 2, v20
	ds_bpermute_b32 v12, v20, v10
	ds_bpermute_b32 v13, v20, v11
	v_xor_b32_e32 v20, 2, v1
	v_cmp_lt_i32_e32 vcc, v20, v14
	s_waitcnt lgkmcnt(0)
	v_pk_add_f32 v[10:11], v[10:11], v[12:13]
	v_cndmask_b32_e32 v21, v1, v20, vcc
	v_lshlrev_b32_e32 v21, 2, v21
	ds_bpermute_b32 v12, v21, v10
	ds_bpermute_b32 v13, v21, v11
	v_xor_b32_e32 v21, 1, v1
	v_cmp_lt_i32_e32 vcc, v21, v14
	s_waitcnt lgkmcnt(0)
	v_pk_add_f32 v[10:11], v[10:11], v[12:13]
	v_cndmask_b32_e32 v12, v1, v21, vcc
	v_lshlrev_b32_e32 v13, 2, v12
	ds_bpermute_b32 v12, v13, v10
	ds_bpermute_b32 v13, v13, v11
	v_cmp_eq_u32_e32 vcc, 0, v17
	s_and_saveexec_b64 s[2:3], vcc
	s_cbranch_execz .LBB0_22
	v_mov_b32_e32 v22, 0
	s_waitcnt lgkmcnt(0)
	v_pk_add_f32 v[10:11], v[10:11], v[12:13]
	global_store_dwordx2 v22, v[10:11], s[4:5] offset:1024

.LBB0_23:
	s_or_b64 exec, exec, s[0:1]
	v_max_f32_e32 v3, v3, v3
	v_max_f32_e32 v2, v2, v2
	v_max_f32_e32 v2, v2, v3
	v_max_f32_e32 v3, v5, v5
	v_max_f32_e32 v4, v4, v4
	v_max_f32_e32 v3, v4, v3
	v_max3_f32 v2, v2, 0, v3
	v_max_f32_e32 v3, v7, v7
	v_max_f32_e32 v4, v6, v6
	v_max_f32_e32 v3, v4, v3
	v_max_f32_e32 v4, v9, v9
	v_max_f32_e32 v5, v8, v8
	v_max_f32_e32 v4, v5, v4
	v_max3_f32 v2, v2, v3, v4
	s_nop 1
	v_max_f32_dpp v3, v2, v2 quad_perm:[1,0,3,2] row_mask:0xf bank_mask:0xf
	s_nop 1
	v_max_f32_dpp v2, v3, v3 quad_perm:[2,3,0,1] row_mask:0xf bank_mask:0xf
	s_nop 1
	v_max_f32_dpp v3, v2, v2 row_ror:4 row_mask:0xf bank_mask:0xf
	s_nop 1
	v_max_f32_dpp v2, v3, v3 row_ror:8 row_mask:0xf bank_mask:0xf
	s_nop 1
	v_readlane_b32 s80, v2, 0
	v_readlane_b32 s81, v2, 16
	v_readlane_b32 s82, v2, 32
	v_readlane_b32 s83, v2, 48
	s_nop 1
	v_mov_b32_e32 v2, s80
	s_nop 0
	v_max_f32_e32 v2, s81, v2
	v_max_f32_e32 v2, s82, v2
	v_max_f32_e32 v2, s83, v2
	v_mov_b32_e32 v1, v2
	v_cmp_eq_u32_e32 vcc, 0, v17
	s_and_saveexec_b64 s[0:1], vcc
	s_cbranch_execz .LBB0_25
	v_lshrrev_b32_e32 v3, 6, v0
	s_waitcnt lgkmcnt(0)
	v_max_f32_e32 v1, v1, v1
	v_max_f32_e32 v2, v2, v2
	v_lshlrev_b32_e32 v3, 2, v3
	v_max_f32_e32 v1, v2, v1
	ds_write_b32 v3, v1 offset:46080
